# v32 + stacked latency cuts (queue claim wait deferred, leader acquire with release, batched rel_bias loads, pj gain pointer from SGPRs, at_dil keeps LDS rel_bias)
# speedup vs baseline: 1.0270x; 1.0027x over previous
; __device__ __forceinline__ void at_dil(const Args& a, LAS unsigned char* lds, int layer) {
;     ...
;     { const int l64 = tid & 63;
;       float g2 = fabsf(a.in[I_QGD][layer * 64 + l64]), g3 = fabsf(a.in[I_KGD][layer * 64 + l64]);
;       float rbm = 0.f;
;       for (int i = l64; i < 32 * 6; i += 64) rbm = fmaxf(rbm, a.in[I_RELB][i]);
; #pragma unroll
;       for (int o2 = 1; o2 < 64; o2 <<= 1) { g2 = fmaxf(g2, __shfl_xor(g2, o2)); g3 = fmaxf(g3, __shfl_xor(g3, o2)); rbm = fmaxf(rbm, __shfl_xor(rbm, o2)); }
;       bdil = 8.f * g2 * g3 * LOG2E * 1.01f; bmax = fmaxf(rbm, 0.f) * LOG2E; }
;     const bool dil_fixed = (bdil + bmax) < 40.f;
;     const float m_dil = bdil + bmax;
;     const unsigned l0 = (unsigned)(uintptr_t)lds;
;     __syncthreads();
;     if (tid < 32 * 6) relb[tid] = a.in[I_RELB][tid] * LOG2E;
.LBB0_527:
	global_load_dword v8, v[2:3], off
	global_load_dword v9, v[2:3], off offset:256
	global_load_dword v10, v[2:3], off offset:512
	v_max_f32_e32 v6, v6, v6
	s_waitcnt vmcnt(0)
	v_max_f32_e32 v8, v8, v8
	v_max_f32_e32 v6, v6, v8
	v_max_f32_e32 v9, v9, v9
	v_max_f32_e32 v6, v6, v9
	v_max_f32_e32 v10, v10, v10
	v_max_f32_e32 v6, v6, v10
	s_or_b64 exec, exec, s[4:5]
	v_and_b32_e32 v2, 0x7fffffff, v5
	ds_bpermute_b32 v2, v156, v2
	v_and_b32_e32 v3, 0x7fffffff, v4
	ds_bpermute_b32 v3, v156, v3
	ds_bpermute_b32 v7, v156, v6
	v_max_f32_e64 v5, |v5|, |v5|
	s_waitcnt lgkmcnt(2)
	v_max_f32_e32 v2, v2, v2
	v_max_f32_e32 v2, v5, v2
	s_waitcnt lgkmcnt(1)
	v_max_f32_e32 v3, v3, v3
	v_max_f32_e64 v4, |v4|, |v4|
	v_max_f32_e32 v3, v4, v3
	ds_bpermute_b32 v4, v158, v2
	s_waitcnt lgkmcnt(1)
	v_max_f32_e32 v5, v7, v7
	v_max_f32_e32 v6, v6, v6
	ds_bpermute_b32 v7, v158, v3
	v_max_f32_e32 v5, v6, v5
	ds_bpermute_b32 v6, v158, v5
	s_waitcnt lgkmcnt(2)
	v_max_f32_e32 v4, v4, v4
	v_max_f32_e32 v2, v2, v4
	s_waitcnt lgkmcnt(1)
	v_max_f32_e32 v4, v7, v7
	ds_bpermute_b32 v7, v159, v2
	v_max_f32_e32 v3, v3, v4
	s_waitcnt lgkmcnt(1)
	v_max_f32_e32 v4, v6, v6
	ds_bpermute_b32 v6, v159, v3
	v_max_f32_e32 v4, v5, v4
	s_waitcnt lgkmcnt(1)
	v_max_f32_e32 v5, v7, v7
	ds_bpermute_b32 v7, v159, v4
	v_max_f32_e32 v2, v2, v5
	s_waitcnt lgkmcnt(1)
	v_max_f32_e32 v5, v6, v6
	ds_bpermute_b32 v6, v160, v2
	v_max_f32_e32 v3, v3, v5
	s_waitcnt lgkmcnt(1)
	v_max_f32_e32 v5, v7, v7
	ds_bpermute_b32 v7, v160, v3
	v_max_f32_e32 v4, v4, v5
	s_waitcnt lgkmcnt(1)
	v_max_f32_e32 v5, v6, v6
	ds_bpermute_b32 v6, v160, v4
	v_max_f32_e32 v2, v2, v5
	s_waitcnt lgkmcnt(1)
	v_max_f32_e32 v5, v7, v7
	v_max_f32_e32 v3, v3, v5
	ds_bpermute_b32 v5, v250, v2
	s_waitcnt lgkmcnt(1)
	v_max_f32_e32 v6, v6, v6
	ds_bpermute_b32 v7, v250, v3
	v_max_f32_e32 v6, v4, v6
	ds_bpermute_b32 v8, v250, v6
	s_waitcnt lgkmcnt(2)
	v_max_f32_e32 v4, v5, v5
	v_max_f32_e32 v2, v2, v4
	s_waitcnt lgkmcnt(1)
	v_max_f32_e32 v4, v7, v7
	v_max_f32_e32 v4, v3, v4
	s_waitcnt lgkmcnt(0)
	v_max_f32_e32 v3, v8, v8
	v_max_f32_e32 v5, v6, v3
	ds_bpermute_b32 v3, v251, v2
	ds_bpermute_b32 v6, v251, v4
	ds_bpermute_b32 v7, v251, v5
	s_movk_i32 s2, 0
	v_cmp_gt_i32_e32 vcc, s2, v18
	s_waitcnt lgkmcnt(0)
	s_barrier
	s_and_saveexec_b64 s[4:5], vcc
	s_cbranch_execz .LBB0_530
	v_readlane_b32 s8, v252, 41
	v_ashrrev_i32_e32 v19, 31, v18
	v_readlane_b32 s9, v252, 42
	v_readlane_b32 s10, v252, 43
	v_readlane_b32 s11, v252, 44
	v_lshl_add_u64 v[8:9], v[18:19], 2, s[8:9]
	global_load_dword v8, v[8:9], off
	v_lshl_add_u32 v9, v18, 2, 0
	v_add_u32_e32 v9, 0x21f00, v9
	v_readlane_b32 s12, v252, 45
	v_readlane_b32 s13, v252, 46
	v_readlane_b32 s14, v252, 47
	v_readlane_b32 s15, v252, 48
	s_waitcnt vmcnt(0)
	v_mul_f32_e32 v8, 0x3fb8aa3b, v8
	ds_write_b32 v9, v8
